# gate|up K-loop: LDS-DMA staging rebalanced to 4+4 pieces per load phase (Bs[b][1] half-tile staged one load phase later, waits vmcnt 8/6)
# speedup vs baseline: 1.0027x; 1.0027x over previous
; #define PG8_STAGE(bufoff, gbase, voff) do { _Pragma("unroll") for (int _i = 0; _i < 2; ++_i) \
;         __builtin_amdgcn_global_load_lds((const unsigned*)((const char*)(gbase) + (voff)[_i]), (PG8_LAS unsigned*)(lds + (bufoff) + ldsw + _i * 8192), 16, 0, 0); } while (0)
; #define PG8_LDA(dst, b, h) do { _Pragma("unroll") for (int m = 0; m < 4; ++m) _Pragma("unroll") for (int k = 0; k < 2; ++k) dst[m][k] = *(const PG8_LAS bf16x8*)(lds + PG8_SA(b, h) + aoff + m * 2048 + k * 1024); } while (0)
; #define PG8_LDB(dst, b, h) do { _Pragma("unroll") for (int n = 0; n < 2; ++n) _Pragma("unroll") for (int k = 0; k < 2; ++k) dst[n][k] = *(const PG8_LAS bf16x8*)(lds + PG8_SB(b, h) + boff + n * 2048 + k * 1024); } while (0)
; #define PG8_MMA(ai, bj, At, Bt) do { __builtin_amdgcn_s_setprio(1); _Pragma("unroll") for (int m = 0; m < 4; ++m) _Pragma("unroll") for (int n = 0; n < 2; ++n) _Pragma("unroll") for (int k = 0; k < 2; ++k) \
;         acc[ai][bj][m][n] = __builtin_amdgcn_mfma_f32_16x16x32_bf16(Bt[n][k], At[m][k], acc[ai][bj][m][n], 0, 0, 0); __builtin_amdgcn_s_setprio(0); } while (0)
; #define PG8_WAIT_V(n) asm volatile("s_waitcnt vmcnt(" #n ")" ::: "memory")
; #define PG8_WAIT_L(n) asm volatile("s_waitcnt lgkmcnt(" #n ")" ::: "memory")
; #define PG8_BAR __builtin_amdgcn_s_barrier()
; template <class Epi, class Sched, bool ALIGN_EPI>
; __device__ __forceinline__ void gemm_phase(PG8_LAS unsigned char* lds, const Gemm g, const Sched& S, const Epi& E, const int tid) {
;     ...
;             const bool last = (t == nt - 2);
;             const char* a1 = cA + (size_t)(t + 1) * kstepA;
;             const char* a2 = last ? nA : cA + (size_t)(t + 2) * kstepA; const char* b2 = last ? nB : cB + (size_t)(t + 2) * kstepB;
;             const char* a3 = a2 + kstepA; const char* b3 = b2 + kstepB;
;             if (last && has_next) S.a_ready(nxt);
;             PG8_LDB(B0, 0, 0); PG8_LDB(B1, 0, 1); PG8_SCHED; PG8_LDA(At, 0, 0); PG8_STAGE(PG8_SA(1, 1), a1 + hstepA, voffA);
;             PG8_WAIT_V(8); PG8_WAIT_L(0); PG8_BAR; PG8_MMA(0, 0, At, B0); PG8_MMA(0, 1, At, B1); PG8_BAR; PG8_SCHED;
;             PG8_LDA(At, 0, 1); PG8_STAGE(PG8_SB(0, 0), b2, voffB); PG8_STAGE(PG8_SB(0, 1), b2 + hstepB, voffB); PG8_STAGE(PG8_SA(0, 0), a2, voffA);
;             PG8_WAIT_V(8); PG8_WAIT_L(0); PG8_BAR; PG8_MMA(1, 0, At, B0); PG8_MMA(1, 1, At, B1); PG8_BAR; PG8_SCHED;
.LBB0_246:
	s_add_u32 s18, s16, 0x4000
	s_addc_u32 s19, s17, 0
	s_cmp_eq_u32 s62, 28
	s_cselect_b32 s22, s58, s18
	s_cselect_b32 s23, s11, s19
	s_cselect_b32 s20, s59, s60
	s_cselect_b32 s21, s9, s61
	s_add_u32 s18, s22, 0x8000
	s_addc_u32 s19, s23, 0
	s_add_i32 s63, 0, 0x10000
	s_add_i32 s66, 0, 0x14000
	s_sub_u32 s98, s60, 0x4000
	s_subb_u32 s99, s61, 0
	ds_read_b128 v[80:83], v166
	ds_read_b128 v[84:87], v166 offset:1024
	ds_read_b128 v[96:99], v166 offset:2048
	ds_read_b128 v[100:103], v166 offset:3072
	ds_read_b128 v[162:165], v166 offset:16384
	ds_read_b128 v[182:185], v166 offset:17408
	ds_read_b128 v[186:189], v166 offset:18432
	ds_read_b128 v[190:193], v166 offset:19456
	s_add_i32 m0, s42, 0x1c000
	ds_read_b128 v[194:197], v180
	ds_read_b128 v[198:201], v180 offset:1024
	ds_read_b128 v[202:205], v180 offset:2048
	ds_read_b128 v[206:209], v180 offset:3072
	ds_read_b128 v[210:213], v180 offset:4096
	ds_read_b128 v[214:217], v180 offset:5120
	ds_read_b128 v[218:221], v180 offset:6144
	ds_read_b128 v[222:225], v180 offset:7168
	global_load_lds_dwordx4 v150, s[98:99]
	s_add_i32 m0, s42, 0x1e000
	s_nop 0
	global_load_lds_dwordx4 v146, s[98:99]
	s_add_i32 m0, s45, 0xc000
	s_nop 0
	global_load_lds_dwordx4 v158, s[16:17]
	s_add_i32 m0, s45, 0xe000
	s_nop 0
	global_load_lds_dwordx4 v160, s[16:17]
	s_waitcnt vmcnt(8)
	s_waitcnt lgkmcnt(0)
	s_setprio 1
	s_barrier
	v_mfma_f32_16x16x32_bf16 v[142:145], v[80:83], v[194:197], v[142:145]
	v_mfma_f32_16x16x32_bf16 v[134:137], v[96:99], v[194:197], v[134:137]
	v_mfma_f32_16x16x32_bf16 v[124:127], v[80:83], v[202:205], v[124:127]
	v_mfma_f32_16x16x32_bf16 v[116:119], v[96:99], v[202:205], v[116:119]
	v_mfma_f32_16x16x32_bf16 v[108:111], v[80:83], v[210:213], v[108:111]
	v_mfma_f32_16x16x32_bf16 v[92:95], v[96:99], v[210:213], v[92:95]
	v_mfma_f32_16x16x32_bf16 v[76:79], v[80:83], v[218:221], v[76:79]
	v_mfma_f32_16x16x32_bf16 v[68:71], v[96:99], v[218:221], v[68:71]
	v_mfma_f32_16x16x32_bf16 v[142:145], v[84:87], v[198:201], v[142:145]
	v_mfma_f32_16x16x32_bf16 v[134:137], v[100:103], v[198:201], v[134:137]
	v_mfma_f32_16x16x32_bf16 v[124:127], v[84:87], v[206:209], v[124:127]
	v_mfma_f32_16x16x32_bf16 v[116:119], v[100:103], v[206:209], v[116:119]
	v_mfma_f32_16x16x32_bf16 v[108:111], v[84:87], v[214:217], v[108:111]
	v_mfma_f32_16x16x32_bf16 v[92:95], v[100:103], v[214:217], v[92:95]
	v_mfma_f32_16x16x32_bf16 v[76:79], v[84:87], v[222:225], v[76:79]
	v_mfma_f32_16x16x32_bf16 v[68:71], v[100:103], v[222:225], v[68:71]
	v_mfma_f32_16x16x32_bf16 v[138:141], v[162:165], v[194:197], v[138:141]
	v_mfma_f32_16x16x32_bf16 v[130:133], v[186:189], v[194:197], v[130:133]
	v_mfma_f32_16x16x32_bf16 v[120:123], v[162:165], v[202:205], v[120:123]
	v_mfma_f32_16x16x32_bf16 v[112:115], v[186:189], v[202:205], v[112:115]
	v_mfma_f32_16x16x32_bf16 v[104:107], v[162:165], v[210:213], v[104:107]
	v_mfma_f32_16x16x32_bf16 v[88:91], v[186:189], v[210:213], v[88:91]
	v_mfma_f32_16x16x32_bf16 v[72:75], v[162:165], v[218:221], v[72:75]
	v_mfma_f32_16x16x32_bf16 v[64:67], v[186:189], v[218:221], v[64:67]
	v_mfma_f32_16x16x32_bf16 v[138:141], v[182:185], v[198:201], v[138:141]
	v_mfma_f32_16x16x32_bf16 v[130:133], v[190:193], v[198:201], v[130:133]
	v_mfma_f32_16x16x32_bf16 v[120:123], v[182:185], v[206:209], v[120:123]
	v_mfma_f32_16x16x32_bf16 v[112:115], v[190:193], v[206:209], v[112:115]
	v_mfma_f32_16x16x32_bf16 v[104:107], v[182:185], v[214:217], v[104:107]
	v_mfma_f32_16x16x32_bf16 v[88:91], v[190:193], v[214:217], v[88:91]
	v_mfma_f32_16x16x32_bf16 v[72:75], v[182:185], v[222:225], v[72:75]
	v_mfma_f32_16x16x32_bf16 v[64:67], v[190:193], v[222:225], v[64:67]
	s_barrier
	s_setprio 0
	s_add_i32 s63, s63, s42
	s_mov_b32 m0, s63
	ds_read_b128 v[194:197], v180 offset:16384
	ds_read_b128 v[198:201], v180 offset:17408
	ds_read_b128 v[202:205], v180 offset:18432
	ds_read_b128 v[206:209], v180 offset:19456
	ds_read_b128 v[210:213], v180 offset:20480
	ds_read_b128 v[214:217], v180 offset:21504
	ds_read_b128 v[218:221], v180 offset:22528
	ds_read_b128 v[222:225], v180 offset:23552
	global_load_lds_dwordx4 v150, s[20:21]
	s_add_i32 m0, s63, 0x2000
	s_nop 0
	global_load_lds_dwordx4 v146, s[20:21]
	s_mov_b32 m0, s45
	s_nop 0
	global_load_lds_dwordx4 v152, s[22:23]
	s_mov_b32 m0, s46
	s_nop 0
	global_load_lds_dwordx4 v148, s[22:23]
	s_waitcnt vmcnt(6)
	s_waitcnt lgkmcnt(0)
	s_setprio 1
	s_barrier
	v_mfma_f32_16x16x32_bf16 v[60:63], v[80:83], v[194:197], v[60:63]
	v_mfma_f32_16x16x32_bf16 v[52:55], v[96:99], v[194:197], v[52:55]
	v_mfma_f32_16x16x32_bf16 v[44:47], v[80:83], v[202:205], v[44:47]
	v_mfma_f32_16x16x32_bf16 v[36:39], v[96:99], v[202:205], v[36:39]
	v_mfma_f32_16x16x32_bf16 v[28:31], v[80:83], v[210:213], v[28:31]
	v_mfma_f32_16x16x32_bf16 v[20:23], v[96:99], v[210:213], v[20:23]
	v_mfma_f32_16x16x32_bf16 v[12:15], v[80:83], v[218:221], v[12:15]
	v_mfma_f32_16x16x32_bf16 v[4:7], v[96:99], v[218:221], v[4:7]
	v_mfma_f32_16x16x32_bf16 v[60:63], v[84:87], v[198:201], v[60:63]
	v_mfma_f32_16x16x32_bf16 v[52:55], v[100:103], v[198:201], v[52:55]
	v_mfma_f32_16x16x32_bf16 v[44:47], v[84:87], v[206:209], v[44:47]
	v_mfma_f32_16x16x32_bf16 v[36:39], v[100:103], v[206:209], v[36:39]
	v_mfma_f32_16x16x32_bf16 v[28:31], v[84:87], v[214:217], v[28:31]
	v_mfma_f32_16x16x32_bf16 v[20:23], v[100:103], v[214:217], v[20:23]
	v_mfma_f32_16x16x32_bf16 v[12:15], v[84:87], v[222:225], v[12:15]
	v_mfma_f32_16x16x32_bf16 v[4:7], v[100:103], v[222:225], v[4:7]
	v_mfma_f32_16x16x32_bf16 v[56:59], v[162:165], v[194:197], v[56:59]
	v_mfma_f32_16x16x32_bf16 v[48:51], v[186:189], v[194:197], v[48:51]
	v_mfma_f32_16x16x32_bf16 v[40:43], v[162:165], v[202:205], v[40:43]
	v_mfma_f32_16x16x32_bf16 v[32:35], v[186:189], v[202:205], v[32:35]
	v_mfma_f32_16x16x32_bf16 v[24:27], v[162:165], v[210:213], v[24:27]
	v_mfma_f32_16x16x32_bf16 v[16:19], v[186:189], v[210:213], v[16:19]
	v_mfma_f32_16x16x32_bf16 v[8:11], v[162:165], v[218:221], v[8:11]
	v_mfma_f32_16x16x32_bf16 v[0:3], v[186:189], v[218:221], v[0:3]
	v_mfma_f32_16x16x32_bf16 v[56:59], v[182:185], v[198:201], v[56:59]
	v_mfma_f32_16x16x32_bf16 v[48:51], v[190:193], v[198:201], v[48:51]
	v_mfma_f32_16x16x32_bf16 v[40:43], v[182:185], v[206:209], v[40:43]
	v_mfma_f32_16x16x32_bf16 v[32:35], v[190:193], v[206:209], v[32:35]
	v_mfma_f32_16x16x32_bf16 v[24:27], v[182:185], v[214:217], v[24:27]
	v_mfma_f32_16x16x32_bf16 v[16:19], v[190:193], v[214:217], v[16:19]
	v_mfma_f32_16x16x32_bf16 v[8:11], v[182:185], v[222:225], v[8:11]
	v_mfma_f32_16x16x32_bf16 v[0:3], v[190:193], v[222:225], v[0:3]
	s_barrier
; #define PG8_STAGE(bufoff, gbase, voff) do { _Pragma("unroll") for (int _i = 0; _i < 2; ++_i) \
;         __builtin_amdgcn_global_load_lds((const unsigned*)((const char*)(gbase) + (voff)[_i]), (PG8_LAS unsigned*)(lds + (bufoff) + ldsw + _i * 8192), 16, 0, 0); } while (0)
; #define PG8_LDA(dst, b, h) do { _Pragma("unroll") for (int m = 0; m < 4; ++m) _Pragma("unroll") for (int k = 0; k < 2; ++k) dst[m][k] = *(const PG8_LAS bf16x8*)(lds + PG8_SA(b, h) + aoff + m * 2048 + k * 1024); } while (0)
; #define PG8_LDB(dst, b, h) do { _Pragma("unroll") for (int n = 0; n < 2; ++n) _Pragma("unroll") for (int k = 0; k < 2; ++k) dst[n][k] = *(const PG8_LAS bf16x8*)(lds + PG8_SB(b, h) + boff + n * 2048 + k * 1024); } while (0)
; #define PG8_MMA(ai, bj, At, Bt) do { __builtin_amdgcn_s_setprio(1); _Pragma("unroll") for (int m = 0; m < 4; ++m) _Pragma("unroll") for (int n = 0; n < 2; ++n) _Pragma("unroll") for (int k = 0; k < 2; ++k) \
;         acc[ai][bj][m][n] = __builtin_amdgcn_mfma_f32_16x16x32_bf16(Bt[n][k], At[m][k], acc[ai][bj][m][n], 0, 0, 0); __builtin_amdgcn_s_setprio(0); } while (0)
; #define PG8_WAIT_V(n) asm volatile("s_waitcnt vmcnt(" #n ")" ::: "memory")
; #define PG8_WAIT_L(n) asm volatile("s_waitcnt lgkmcnt(" #n ")" ::: "memory")
; #define PG8_BAR __builtin_amdgcn_s_barrier()
; #define PG8_SCHED __builtin_amdgcn_sched_barrier(0)
; template <class Epi, class Sched, bool ALIGN_EPI>
; __device__ __forceinline__ void gemm_phase(PG8_LAS unsigned char* lds, const Gemm g, const Sched& S, const Epi& E, const int tid) {
;     ...
;             PG8_LDB(B0, 1, 0); PG8_LDB(B1, 1, 1); PG8_SCHED; PG8_LDA(At, 1, 0); PG8_STAGE(PG8_SA(0, 1), a2 + hstepA, voffA);
;             PG8_WAIT_V(8); PG8_WAIT_L(0); PG8_BAR; PG8_MMA(0, 0, At, B0); PG8_MMA(0, 1, At, B1); PG8_BAR; PG8_SCHED;
;             PG8_LDA(At, 1, 1); PG8_STAGE(PG8_SB(1, 0), b3, voffB); PG8_STAGE(PG8_SB(1, 1), b3 + hstepB, voffB); PG8_STAGE(PG8_SA(1, 0), a3, voffA);
;             PG8_WAIT_V(8); PG8_WAIT_L(0); PG8_BAR; PG8_MMA(1, 0, At, B0); PG8_MMA(1, 1, At, B1); PG8_BAR; PG8_SCHED;
;         }
	s_setprio 0
	s_add_i32 s63, 0, 0x18000
	s_add_i32 s64, 0, 0x1c000
	s_add_u32 s98, s20, 0x4000
	s_addc_u32 s99, s21, 0
	ds_read_b128 v[80:83], v166 offset:32768
	ds_read_b128 v[84:87], v166 offset:33792
	ds_read_b128 v[96:99], v166 offset:34816
	ds_read_b128 v[100:103], v166 offset:35840
	ds_read_b128 v[162:165], v166 offset:49152
	ds_read_b128 v[182:185], v166 offset:50176
	ds_read_b128 v[186:189], v166 offset:51200
	ds_read_b128 v[190:193], v166 offset:52224
	s_add_u32 s22, s22, 0x4000
	s_addc_u32 s23, s23, 0
	s_add_i32 m0, s42, 0x14000
	ds_read_b128 v[194:197], v180 offset:32768
	ds_read_b128 v[198:201], v180 offset:33792
	ds_read_b128 v[202:205], v180 offset:34816
	ds_read_b128 v[206:209], v180 offset:35840
	ds_read_b128 v[210:213], v180 offset:36864
	ds_read_b128 v[214:217], v180 offset:37888
	ds_read_b128 v[218:221], v180 offset:38912
	ds_read_b128 v[222:225], v180 offset:39936
	global_load_lds_dwordx4 v150, s[98:99]
	s_add_i32 m0, s42, 0x16000
	s_nop 0
	global_load_lds_dwordx4 v146, s[98:99]
	s_mov_b32 m0, s47
	s_nop 0
	global_load_lds_dwordx4 v152, s[22:23]
	s_mov_b32 m0, s48
	s_nop 0
	global_load_lds_dwordx4 v148, s[22:23]
	s_waitcnt vmcnt(8)
	s_waitcnt lgkmcnt(0)
	s_setprio 1
	s_barrier
	v_mfma_f32_16x16x32_bf16 v[142:145], v[80:83], v[194:197], v[142:145]
	v_mfma_f32_16x16x32_bf16 v[134:137], v[96:99], v[194:197], v[134:137]
	v_mfma_f32_16x16x32_bf16 v[124:127], v[80:83], v[202:205], v[124:127]
	v_mfma_f32_16x16x32_bf16 v[116:119], v[96:99], v[202:205], v[116:119]
	v_mfma_f32_16x16x32_bf16 v[108:111], v[80:83], v[210:213], v[108:111]
	v_mfma_f32_16x16x32_bf16 v[92:95], v[96:99], v[210:213], v[92:95]
	v_mfma_f32_16x16x32_bf16 v[76:79], v[80:83], v[218:221], v[76:79]
	v_mfma_f32_16x16x32_bf16 v[68:71], v[96:99], v[218:221], v[68:71]
	v_mfma_f32_16x16x32_bf16 v[142:145], v[84:87], v[198:201], v[142:145]
	v_mfma_f32_16x16x32_bf16 v[134:137], v[100:103], v[198:201], v[134:137]
	v_mfma_f32_16x16x32_bf16 v[124:127], v[84:87], v[206:209], v[124:127]
	v_mfma_f32_16x16x32_bf16 v[116:119], v[100:103], v[206:209], v[116:119]
	v_mfma_f32_16x16x32_bf16 v[108:111], v[84:87], v[214:217], v[108:111]
	v_mfma_f32_16x16x32_bf16 v[92:95], v[100:103], v[214:217], v[92:95]
	v_mfma_f32_16x16x32_bf16 v[76:79], v[84:87], v[222:225], v[76:79]
	v_mfma_f32_16x16x32_bf16 v[68:71], v[100:103], v[222:225], v[68:71]
	v_mfma_f32_16x16x32_bf16 v[138:141], v[162:165], v[194:197], v[138:141]
	v_mfma_f32_16x16x32_bf16 v[130:133], v[186:189], v[194:197], v[130:133]
	v_mfma_f32_16x16x32_bf16 v[120:123], v[162:165], v[202:205], v[120:123]
	v_mfma_f32_16x16x32_bf16 v[112:115], v[186:189], v[202:205], v[112:115]
	v_mfma_f32_16x16x32_bf16 v[104:107], v[162:165], v[210:213], v[104:107]
	v_mfma_f32_16x16x32_bf16 v[88:91], v[186:189], v[210:213], v[88:91]
	v_mfma_f32_16x16x32_bf16 v[72:75], v[162:165], v[218:221], v[72:75]
	v_mfma_f32_16x16x32_bf16 v[64:67], v[186:189], v[218:221], v[64:67]
	v_mfma_f32_16x16x32_bf16 v[138:141], v[182:185], v[198:201], v[138:141]
	v_mfma_f32_16x16x32_bf16 v[130:133], v[190:193], v[198:201], v[130:133]
	v_mfma_f32_16x16x32_bf16 v[120:123], v[182:185], v[206:209], v[120:123]
	v_mfma_f32_16x16x32_bf16 v[112:115], v[190:193], v[206:209], v[112:115]
	v_mfma_f32_16x16x32_bf16 v[104:107], v[182:185], v[214:217], v[104:107]
	v_mfma_f32_16x16x32_bf16 v[88:91], v[190:193], v[214:217], v[88:91]
	v_mfma_f32_16x16x32_bf16 v[72:75], v[182:185], v[222:225], v[72:75]
	v_mfma_f32_16x16x32_bf16 v[64:67], v[190:193], v[222:225], v[64:67]
	s_barrier
	s_setprio 0
	s_add_u32 s22, s20, 0x8000
	s_addc_u32 s23, s21, 0
	s_add_i32 s63, s63, s42
	s_mov_b32 m0, s63
	ds_read_b128 v[194:197], v180 offset:49152
	ds_read_b128 v[198:201], v180 offset:50176
	ds_read_b128 v[202:205], v180 offset:51200
	ds_read_b128 v[206:209], v180 offset:52224
	ds_read_b128 v[210:213], v180 offset:53248
	ds_read_b128 v[214:217], v180 offset:54272
	ds_read_b128 v[218:221], v180 offset:55296
	ds_read_b128 v[222:225], v180 offset:56320
	global_load_lds_dwordx4 v150, s[22:23]
	s_add_i32 m0, s63, 0x2000
	s_nop 0
	global_load_lds_dwordx4 v146, s[22:23]
	s_mov_b32 m0, s51
	s_nop 0
	global_load_lds_dwordx4 v152, s[18:19]
	s_mov_b32 m0, s52
	s_nop 0
	global_load_lds_dwordx4 v148, s[18:19]
	s_waitcnt vmcnt(6)
	s_waitcnt lgkmcnt(0)
	s_setprio 1
	s_barrier
	v_mfma_f32_16x16x32_bf16 v[60:63], v[80:83], v[194:197], v[60:63]
	v_mfma_f32_16x16x32_bf16 v[52:55], v[96:99], v[194:197], v[52:55]
	v_mfma_f32_16x16x32_bf16 v[44:47], v[80:83], v[202:205], v[44:47]
	v_mfma_f32_16x16x32_bf16 v[36:39], v[96:99], v[202:205], v[36:39]
	v_mfma_f32_16x16x32_bf16 v[28:31], v[80:83], v[210:213], v[28:31]
	v_mfma_f32_16x16x32_bf16 v[20:23], v[96:99], v[210:213], v[20:23]
	v_mfma_f32_16x16x32_bf16 v[12:15], v[80:83], v[218:221], v[12:15]
	v_mfma_f32_16x16x32_bf16 v[4:7], v[96:99], v[218:221], v[4:7]
	v_mfma_f32_16x16x32_bf16 v[60:63], v[84:87], v[198:201], v[60:63]
	v_mfma_f32_16x16x32_bf16 v[52:55], v[100:103], v[198:201], v[52:55]
	v_mfma_f32_16x16x32_bf16 v[44:47], v[84:87], v[206:209], v[44:47]
	v_mfma_f32_16x16x32_bf16 v[36:39], v[100:103], v[206:209], v[36:39]
	v_mfma_f32_16x16x32_bf16 v[28:31], v[84:87], v[214:217], v[28:31]
	v_mfma_f32_16x16x32_bf16 v[20:23], v[100:103], v[214:217], v[20:23]
	v_mfma_f32_16x16x32_bf16 v[12:15], v[84:87], v[222:225], v[12:15]
	v_mfma_f32_16x16x32_bf16 v[4:7], v[100:103], v[222:225], v[4:7]
	v_mfma_f32_16x16x32_bf16 v[56:59], v[162:165], v[194:197], v[56:59]
	v_mfma_f32_16x16x32_bf16 v[48:51], v[186:189], v[194:197], v[48:51]
	v_mfma_f32_16x16x32_bf16 v[40:43], v[162:165], v[202:205], v[40:43]
	v_mfma_f32_16x16x32_bf16 v[32:35], v[186:189], v[202:205], v[32:35]
	v_mfma_f32_16x16x32_bf16 v[24:27], v[162:165], v[210:213], v[24:27]
	v_mfma_f32_16x16x32_bf16 v[16:19], v[186:189], v[210:213], v[16:19]
	v_mfma_f32_16x16x32_bf16 v[8:11], v[162:165], v[218:221], v[8:11]
	v_mfma_f32_16x16x32_bf16 v[0:3], v[186:189], v[218:221], v[0:3]
	v_mfma_f32_16x16x32_bf16 v[56:59], v[182:185], v[198:201], v[56:59]
	v_mfma_f32_16x16x32_bf16 v[48:51], v[190:193], v[198:201], v[48:51]
	v_mfma_f32_16x16x32_bf16 v[40:43], v[182:185], v[206:209], v[40:43]
	v_mfma_f32_16x16x32_bf16 v[32:35], v[190:193], v[206:209], v[32:35]
	v_mfma_f32_16x16x32_bf16 v[24:27], v[182:185], v[214:217], v[24:27]
	v_mfma_f32_16x16x32_bf16 v[16:19], v[190:193], v[214:217], v[16:19]
	v_mfma_f32_16x16x32_bf16 v[8:11], v[182:185], v[222:225], v[8:11]
	v_mfma_f32_16x16x32_bf16 v[0:3], v[190:193], v[222:225], v[0:3]
	s_barrier
	s_setprio 0
	s_add_i32 s62, s62, 2
	s_add_u32 s16, s16, 0x10000
	s_addc_u32 s17, s17, 0
	s_add_u32 s60, s60, 0x10000
	s_addc_u32 s61, s61, 0
	s_cmp_gt_u32 s62, 29
	s_cbranch_scc0 .LBB0_246
	s_and_b64 vcc, exec, s[6:7]
	s_cbranch_vccz .LBB0_249
	s_barrier

; __global__ void __launch_bounds__(NWAVES * 64, 2) mk_fwd(Args args) {
	.amdhsa_kernel _Z6mk_fwd4Args
		.amdhsa_group_segment_fixed_size 0
		.amdhsa_private_segment_fixed_size 0
		.amdhsa_kernarg_size 400
		.amdhsa_user_sgpr_count 2
		.amdhsa_user_sgpr_dispatch_ptr 0
		.amdhsa_user_sgpr_queue_ptr 0
		.amdhsa_user_sgpr_kernarg_segment_ptr 1
		.amdhsa_user_sgpr_dispatch_id 0
		.amdhsa_user_sgpr_kernarg_preload_length 0
		.amdhsa_user_sgpr_kernarg_preload_offset 0
		.amdhsa_user_sgpr_private_segment_size 0
		.amdhsa_uses_dynamic_stack 0
		.amdhsa_enable_private_segment 0
		.amdhsa_system_sgpr_workgroup_id_x 1
		.amdhsa_system_sgpr_workgroup_id_y 0
		.amdhsa_system_sgpr_workgroup_id_z 0
		.amdhsa_system_sgpr_workgroup_info 0
		.amdhsa_system_vgpr_workitem_id 0
		.amdhsa_next_free_vgpr 256
		.amdhsa_next_free_sgpr 100
		.amdhsa_accum_offset 256
		.amdhsa_reserve_vcc 1
		.amdhsa_float_round_mode_32 0
		.amdhsa_float_round_mode_16_64 0
		.amdhsa_float_denorm_mode_32 3
		.amdhsa_float_denorm_mode_16_64 3
		.amdhsa_dx10_clamp 1
		.amdhsa_ieee_mode 1
		.amdhsa_fp16_overflow 0
		.amdhsa_tg_split 0
		.amdhsa_exception_fp_ieee_invalid_op 0
		.amdhsa_exception_fp_denorm_src 0
		.amdhsa_exception_fp_ieee_div_zero 0
		.amdhsa_exception_fp_ieee_overflow 0
		.amdhsa_exception_fp_ieee_underflow 0
		.amdhsa_exception_fp_ieee_inexact 0
		.amdhsa_exception_int_div_zero 0
	.end_amdhsa_kernel

; __global__ void __launch_bounds__(NWAVES * 64, 2) mk_fwd(Args args) {
amdhsa.kernels:
  - .agpr_count:     0
    .args:
      - .offset:         0
        .size:           144
        .value_kind:     by_value
      - .offset:         144
        .size:           4
        .value_kind:     hidden_block_count_x
      - .offset:         148
        .size:           4
        .value_kind:     hidden_block_count_y
      - .offset:         152
        .size:           4
        .value_kind:     hidden_block_count_z
      - .offset:         156
        .size:           2
        .value_kind:     hidden_group_size_x
      - .offset:         158
        .size:           2
        .value_kind:     hidden_group_size_y
      - .offset:         160
        .size:           2
        .value_kind:     hidden_group_size_z
      - .offset:         162
        .size:           2
        .value_kind:     hidden_remainder_x
      - .offset:         164
        .size:           2
        .value_kind:     hidden_remainder_y
      - .offset:         166
        .size:           2
        .value_kind:     hidden_remainder_z
      - .offset:         184
        .size:           8
        .value_kind:     hidden_global_offset_x
      - .offset:         192
        .size:           8
        .value_kind:     hidden_global_offset_y
      - .offset:         200
        .size:           8
        .value_kind:     hidden_global_offset_z
      - .offset:         208
        .size:           2
        .value_kind:     hidden_grid_dims
      - .offset:         264
        .size:           4
        .value_kind:     hidden_dynamic_lds_size
    .group_segment_fixed_size: 0
    .kernarg_segment_align: 8
    .kernarg_segment_size: 400
    .language:       OpenCL C
    .language_version:
      - 2
      - 0
    .max_flat_workgroup_size: 512
    .name:           _Z6mk_fwd4Args
    .private_segment_fixed_size: 0
    .sgpr_count:     106
    .sgpr_spill_count: 424
    .symbol:         _Z6mk_fwd4Args.kd
    .uniform_work_group_size: 1
    .uses_dynamic_stack: false
    .vgpr_count:     256
    .vgpr_spill_count: 0
    .wavefront_size: 64
